# speedup vs baseline: 1.0030x; 1.0030x over previous
.LBB1_117:
	s_cmp_lt_u32 s37, 10
	s_cselect_b32 s12, 2, -10
	s_add_i32 s12, s12, s37
	s_lshl_b32 s13, s12, 7
	s_add_u32 s14, s13, s52
	s_addc_u32 s15, 0, s53
	s_lshl_b32 s12, s12, 8
	s_add_u32 s12, s8, s12
	s_addc_u32 s13, s9, 0
	s_and_b32 s38, s36, 0x10000
	s_xor_b32 s39, s38, 0x10000
	v_or_b32_e32 v210, s38, v237
	v_mov_b32_e32 v194, v202
	v_add_u32_e32 v196, s39, v239
	v_add_u32_e32 v197, s39, v240
	v_add_u32_e32 v216, s39, v241
	v_add_u32_e32 v217, s39, v242
	v_or_b32_e32 v218, s38, v238
	v_add_u32_e32 v220, v210, v236
	ds_read_b128 v[186:189], v218 offset:32768
	ds_read_b128 v[190:193], v218 offset:34816
	ds_read_b128 v[182:185], v218 offset:36864
	ds_read_b128 v[178:181], v218 offset:38912
	ds_read_b128 v[244:247], v220
	ds_read_b128 v[248:251], v220 offset:2048
	ds_read_b128 v[252:255], v220 offset:4096
	ds_read_b128 v[210:213], v220 offset:6144
	s_waitcnt lgkmcnt(3)
	v_mfma_f32_16x16x32_f16 v[170:173], v[244:247], v[186:189], v[170:173]
	v_mfma_f32_16x16x32_f16 v[162:165], v[244:247], v[190:193], v[162:165]
	v_mfma_f32_16x16x32_f16 v[174:177], v[244:247], v[182:185], v[174:177]
	v_mfma_f32_16x16x32_f16 v[166:169], v[244:247], v[178:181], v[166:169]
	ds_read_b128 v[244:247], v220 offset:8192
	s_waitcnt vmcnt(11)
	ds_write_b128 v196, v[2:5]
	global_load_dwordx4 v[2:5], v198, s[14:15]
	s_waitcnt lgkmcnt(4)
	v_mfma_f32_16x16x32_f16 v[154:157], v[248:251], v[186:189], v[154:157]
	v_mfma_f32_16x16x32_f16 v[146:149], v[248:251], v[190:193], v[146:149]
	v_mfma_f32_16x16x32_f16 v[158:161], v[248:251], v[182:185], v[158:161]
	v_mfma_f32_16x16x32_f16 v[150:153], v[248:251], v[178:181], v[150:153]
	ds_read_b128 v[248:251], v220 offset:10240
	s_waitcnt vmcnt(11)
	ds_write_b128 v197, v[6:9]
	global_load_dwordx4 v[6:9], v199, s[14:15]
	s_waitcnt lgkmcnt(5)
	v_mfma_f32_16x16x32_f16 v[138:141], v[252:255], v[186:189], v[138:141]
	v_mfma_f32_16x16x32_f16 v[130:133], v[252:255], v[190:193], v[130:133]
	v_mfma_f32_16x16x32_f16 v[142:145], v[252:255], v[182:185], v[142:145]
	v_mfma_f32_16x16x32_f16 v[134:137], v[252:255], v[178:181], v[134:137]
	ds_read_b128 v[252:255], v220 offset:12288
	s_waitcnt vmcnt(11)
	ds_write_b128 v196, v[10:13] offset:2048
	global_load_dwordx4 v[10:13], v200, s[14:15]
	s_waitcnt lgkmcnt(6)
	v_mfma_f32_16x16x32_f16 v[122:125], v[210:213], v[186:189], v[122:125]
	v_mfma_f32_16x16x32_f16 v[114:117], v[210:213], v[190:193], v[114:117]
	v_mfma_f32_16x16x32_f16 v[126:129], v[210:213], v[182:185], v[126:129]
	v_mfma_f32_16x16x32_f16 v[118:121], v[210:213], v[178:181], v[118:121]
	ds_read_b128 v[210:213], v220 offset:14336
	s_waitcnt vmcnt(11)
	ds_write_b128 v197, v[14:17] offset:2048
	global_load_dwordx4 v[14:17], v201, s[14:15]
	s_waitcnt lgkmcnt(7)
	v_mfma_f32_16x16x32_f16 v[106:109], v[244:247], v[186:189], v[106:109]
	v_lshl_add_u64 v[196:197], s[12:13], 0, v[194:195]
	v_mfma_f32_16x16x32_f16 v[98:101], v[244:247], v[190:193], v[98:101]
	v_mfma_f32_16x16x32_f16 v[110:113], v[244:247], v[182:185], v[110:113]
	v_mfma_f32_16x16x32_f16 v[102:105], v[244:247], v[178:181], v[102:105]
	ds_read_b128 v[244:247], v220 offset:1024
	s_waitcnt vmcnt(11)
	v_cvt_pk_f16_f32 v25, v24, v25
	v_cvt_pk_f16_f32 v24, v22, v23
	ds_write_b64 v216, v[24:25]
	global_load_dwordx4 v[22:25], v194, s[12:13] nt
	s_waitcnt lgkmcnt(7)
	v_mfma_f32_16x16x32_f16 v[90:93], v[248:251], v[186:189], v[90:93]
	v_mfma_f32_16x16x32_f16 v[82:85], v[248:251], v[190:193], v[82:85]
	v_mfma_f32_16x16x32_f16 v[94:97], v[248:251], v[182:185], v[94:97]
	v_mfma_f32_16x16x32_f16 v[86:89], v[248:251], v[178:181], v[86:89]
	ds_read_b128 v[248:251], v220 offset:3072
	s_waitcnt vmcnt(11)
	v_cvt_pk_f16_f32 v21, v20, v21
	v_cvt_pk_f16_f32 v20, v18, v19
	ds_write_b64 v216, v[20:21] offset:1024
	global_load_dwordx4 v[18:21], v194, s[12:13] offset:128 nt
	s_waitcnt lgkmcnt(7)
	v_mfma_f32_16x16x32_f16 v[74:77], v[252:255], v[186:189], v[74:77]
	v_add_co_u32_e32 v214, vcc, s23, v196
	v_mfma_f32_16x16x32_f16 v[66:69], v[252:255], v[190:193], v[66:69]
	s_nop 0
	v_addc_co_u32_e32 v215, vcc, 0, v197, vcc
	v_mfma_f32_16x16x32_f16 v[78:81], v[252:255], v[182:185], v[78:81]
	v_mfma_f32_16x16x32_f16 v[70:73], v[252:255], v[178:181], v[70:73]
	ds_read_b128 v[252:255], v220 offset:5120
	s_waitcnt vmcnt(11)
	v_cvt_pk_f16_f32 v33, v32, v33
	v_cvt_pk_f16_f32 v32, v30, v31
	ds_write_b64 v217, v[32:33]
	global_load_dwordx4 v[30:33], v[214:215], off nt
	s_waitcnt lgkmcnt(7)
	v_mfma_f32_16x16x32_f16 v[62:65], v[210:213], v[186:189], v[62:65]
	ds_read_b128 v[186:189], v220 offset:7168
	s_waitcnt vmcnt(11)
	v_mfma_f32_16x16x32_f16 v[58:61], v[210:213], v[182:185], v[58:61]
	v_cvt_pk_f16_f32 v183, v28, v29
	v_cvt_pk_f16_f32 v182, v26, v27
	global_load_dwordx4 v[26:29], v[214:215], off offset:128 nt
	v_mfma_f32_16x16x32_f16 v[54:57], v[210:213], v[190:193], v[54:57]
	ds_write_b64 v217, v[182:183] offset:1024
	v_mfma_f32_16x16x32_f16 v[50:53], v[210:213], v[178:181], v[50:53]
	ds_read_b128 v[178:181], v218 offset:33792
	ds_read_b128 v[182:185], v218 offset:35840
	ds_read_b128 v[190:193], v218 offset:37888
	ds_read_b128 v[210:213], v218 offset:39936
	s_waitcnt lgkmcnt(3)
	v_mfma_f32_16x16x32_f16 v[170:173], v[244:247], v[178:181], v[170:173]
	v_add_co_u32_e32 v214, vcc, s24, v196
	s_waitcnt lgkmcnt(2)
	v_mfma_f32_16x16x32_f16 v[162:165], v[244:247], v[182:185], v[162:165]
	v_addc_co_u32_e32 v215, vcc, 0, v197, vcc
	s_waitcnt lgkmcnt(1)
	v_mfma_f32_16x16x32_f16 v[174:177], v[244:247], v[190:193], v[174:177]
	s_waitcnt lgkmcnt(0)
	v_mfma_f32_16x16x32_f16 v[166:169], v[244:247], v[210:213], v[166:169]
	ds_read_b128 v[244:247], v220 offset:9216
	s_waitcnt vmcnt(11)
	v_cvt_pk_f16_f32 v41, v40, v41
	v_cvt_pk_f16_f32 v40, v38, v39
	ds_write_b64 v216, v[40:41] offset:2048
	global_load_dwordx4 v[38:41], v[214:215], off nt
	v_mfma_f32_16x16x32_f16 v[154:157], v[248:251], v[178:181], v[154:157]
	v_mfma_f32_16x16x32_f16 v[146:149], v[248:251], v[182:185], v[146:149]
	v_mfma_f32_16x16x32_f16 v[158:161], v[248:251], v[190:193], v[158:161]
	v_mfma_f32_16x16x32_f16 v[150:153], v[248:251], v[210:213], v[150:153]
	ds_read_b128 v[248:251], v220 offset:11264
	s_waitcnt vmcnt(11)
	v_cvt_pk_f16_f32 v37, v36, v37
	v_cvt_pk_f16_f32 v36, v34, v35
	ds_write_b64 v216, v[36:37] offset:3072
	global_load_dwordx4 v[34:37], v[214:215], off offset:128 nt
	v_mfma_f32_16x16x32_f16 v[138:141], v[252:255], v[178:181], v[138:141]
	v_add_co_u32_e32 v196, vcc, s25, v196
	v_mfma_f32_16x16x32_f16 v[130:133], v[252:255], v[182:185], v[130:133]
	s_nop 0
	v_addc_co_u32_e32 v197, vcc, 0, v197, vcc
	v_mfma_f32_16x16x32_f16 v[142:145], v[252:255], v[190:193], v[142:145]
	v_mfma_f32_16x16x32_f16 v[134:137], v[252:255], v[210:213], v[134:137]
	ds_read_b128 v[252:255], v220 offset:13312
	s_waitcnt vmcnt(11)
	v_cvt_pk_f16_f32 v49, v48, v49
	v_cvt_pk_f16_f32 v48, v46, v47
	ds_write_b64 v217, v[48:49] offset:2048
	global_load_dwordx4 v[46:49], v[196:197], off nt
	v_mfma_f32_16x16x32_f16 v[122:125], v[186:189], v[178:181], v[122:125]
	v_mfma_f32_16x16x32_f16 v[114:117], v[186:189], v[182:185], v[114:117]
	v_mfma_f32_16x16x32_f16 v[126:129], v[186:189], v[190:193], v[126:129]
	v_mfma_f32_16x16x32_f16 v[118:121], v[186:189], v[210:213], v[118:121]
	ds_read_b128 v[186:189], v220 offset:15360
	s_waitcnt vmcnt(11)
	v_cvt_pk_f16_f32 v45, v44, v45
	v_cvt_pk_f16_f32 v44, v42, v43
	ds_write_b64 v217, v[44:45] offset:3072
	global_load_dwordx4 v[42:45], v[196:197], off offset:128 nt
	s_waitcnt lgkmcnt(7)
	v_mfma_f32_16x16x32_f16 v[106:109], v[244:247], v[178:181], v[106:109]
	v_mfma_f32_16x16x32_f16 v[98:101], v[244:247], v[182:185], v[98:101]
	v_mfma_f32_16x16x32_f16 v[110:113], v[244:247], v[190:193], v[110:113]
	v_mfma_f32_16x16x32_f16 v[102:105], v[244:247], v[210:213], v[102:105]
	s_waitcnt lgkmcnt(5)
	v_mfma_f32_16x16x32_f16 v[90:93], v[248:251], v[178:181], v[90:93]
	v_mfma_f32_16x16x32_f16 v[82:85], v[248:251], v[182:185], v[82:85]
	v_mfma_f32_16x16x32_f16 v[94:97], v[248:251], v[190:193], v[94:97]
	v_mfma_f32_16x16x32_f16 v[86:89], v[248:251], v[210:213], v[86:89]
	s_waitcnt lgkmcnt(3)
	v_mfma_f32_16x16x32_f16 v[74:77], v[252:255], v[178:181], v[74:77]
	v_mfma_f32_16x16x32_f16 v[66:69], v[252:255], v[182:185], v[66:69]
	v_mfma_f32_16x16x32_f16 v[78:81], v[252:255], v[190:193], v[78:81]
	v_mfma_f32_16x16x32_f16 v[70:73], v[252:255], v[210:213], v[70:73]
	s_waitcnt lgkmcnt(1)
	v_mfma_f32_16x16x32_f16 v[62:65], v[186:189], v[178:181], v[62:65]
	v_mfma_f32_16x16x32_f16 v[54:57], v[186:189], v[182:185], v[54:57]
	v_mfma_f32_16x16x32_f16 v[58:61], v[186:189], v[190:193], v[58:61]
	v_mfma_f32_16x16x32_f16 v[50:53], v[186:189], v[210:213], v[50:53]
	s_add_i32 s37, s37, 1
	s_add_i32 s36, s36, 0x10000
	s_cmp_eq_u32 s36, 0xc0000
	s_waitcnt lgkmcnt(0)
	s_barrier
	s_cbranch_scc1 .LBB1_83
